# v65 + in-proj tile order: sigmoid-gate tiles first (rounds 0,1), then rope q/k, gelu u/v, plain v_attn last, so the mixer's inputs are the most recently written
# speedup vs baseline: 1.0062x; 1.0062x over previous
;     __device__ bool next(int i, Unit& u) const { if (!base.next(i >> 1, u)) return false; if (i & 1) { u.pm += MTOK / BM; u.pn += DM / BM; } return true; }
;   __device__ __forceinline__ bool next(int i,AttnUnit&u)const{ if(i>=2||vcu>=256)return false; const int s=vcu&3; u.bh=vcu>>2; u.qb=(i==0)?7-s:s; return true; }
;     __host__ __device__ bool next(int i, Unit& u) const {
;         const int L = i * G + c; if (L >= nwg) return false;
;         int wgid = L; { const int q = nwg / NXCD, r = nwg % NXCD, xcd = wgid % NXCD, off = wgid / NXCD; wgid = (xcd < r ? xcd * (q + 1) : r * (q + 1) + (xcd - r) * q) + off; }
;         const int nig = WGM * nN, gid = wgid / nig, fm = gid * WGM, gsz = (nM - fm) < WGM ? (nM - fm) : WGM;
;         u.pm = fm + ((wgid % nig) % gsz); u.pn = (wgid % nig) / gsz; u.half = 0; return true;
.LBB0_382:
	s_ashr_i32 s4, s21, 31
	s_lshr_b32 s4, s4, 29
	s_add_i32 s4, s21, s4
	s_ashr_i32 s5, s4, 3
	s_and_b32 s4, s4, -8
	s_sub_i32 s4, s21, s4
	s_cmp_lt_i32 s4, 0
	s_movk_i32 s6, 0x91
	s_cselect_b32 s6, s6, 0x90
	s_mul_i32 s4, s4, s6
	s_add_i32 s4, s4, s5
	s_mul_hi_i32 s5, s4, 0x38e38e39
	s_lshr_b32 s6, s5, 31
	s_ashr_i32 s5, s5, 5
	s_add_i32 s5, s5, s6
	s_lshl_b32 s6, s5, 3
	s_mulk_i32 s5, 0x90
	s_sub_i32 s4, s4, s5
	s_bfe_u32 s5, s4, 0x3001c
	s_add_i32 s5, s4, s5
	s_sext_i32_i16 s7, s5
	s_and_b32 s5, s5, 0xfff8
	s_sub_i32 s4, s4, s5
	s_sext_i32_i16 s4, s4
	s_add_i32 s18, s6, s4
	s_ashr_i32 s70, s7, 3
	s_mul_i32 s4, s70, 5
	s_cmp_lt_u32 s70, 12
	s_cbranch_scc0 .Lpn_hi0
	s_mov_b32 s6, 0x1ee6b16a
	s_mov_b32 s7, 0x398a48c
	s_branch .Lpn_go0
.Lpn_hi0:
	s_sub_i32 s4, s4, 60
	s_mov_b32 s6, 0x12818820
	s_mov_b32 s7, 0

;     __device__ bool next(int i, Unit& u) const { if (!base.next(i >> 1, u)) return false; if (i & 1) { u.pm += MTOK / BM; u.pn += DM / BM; } return true; }
;   __device__ __forceinline__ bool next(int i,AttnUnit&u)const{ if(i>=2||vcu>=256)return false; const int s=vcu&3; u.bh=vcu>>2; u.qb=(i==0)?7-s:s; return true; }
;     __host__ __device__ bool next(int i, Unit& u) const {
;         const int L = i * G + c; if (L >= nwg) return false;
;         int wgid = L; { const int q = nwg / NXCD, r = nwg % NXCD, xcd = wgid % NXCD, off = wgid / NXCD; wgid = (xcd < r ? xcd * (q + 1) : r * (q + 1) + (xcd - r) * q) + off; }
;         const int nig = WGM * nN, gid = wgid / nig, fm = gid * WGM, gsz = (nM - fm) < WGM ? (nM - fm) : WGM;
;         u.pm = fm + ((wgid % nig) % gsz); u.pn = (wgid % nig) / gsz; u.half = 0; return true;
; template <class Epi, class Sched, bool ALIGN_EPI = false, bool SP2 = false>
; __device__ __forceinline__ void gemm_phase(PG8_LAS unsigned char* lds, const Gemm g, const Sched& S, const Epi& E) {
;     ...
;         const bool has_next = S.next(ui + 1, nxt);
;         const char* nA = has_next ? (const char*)g.A + (size_t)nxt.pm * tstep + (nxt.half == 2 ? hstep : (size_t)0) : cA; const char* nB = has_next ? (const char*)g.Bt + (size_t)nxt.pn * tstep : cB;
.LBB0_392:
	s_add_i32 s72, s72, 1
	s_mul_i32 s10, s72, s33
	s_add_i32 s10, s10, s21
	s_cmpk_lt_i32 s10, 0x480
	s_cselect_b64 s[64:65], -1, 0
	s_cmpk_gt_i32 s10, 0x47f
	s_cbranch_scc1 .LBB0_394
	s_ashr_i32 s11, s10, 31
	s_lshr_b32 s11, s11, 29
	s_add_i32 s11, s10, s11
	s_ashr_i32 s12, s11, 3
	s_and_b32 s11, s11, -8
	s_sub_i32 s10, s10, s11
	s_cmp_lt_i32 s10, 0
	s_movk_i32 s11, 0x91
	s_cselect_b32 s11, s11, 0x90
	s_mul_i32 s10, s10, s11
	s_add_i32 s10, s10, s12
	s_mul_hi_i32 s11, s10, 0x38e38e39
	s_lshr_b32 s12, s11, 31
	s_ashr_i32 s11, s11, 5
	s_add_i32 s11, s11, s12
	s_lshl_b32 s12, s11, 3
	s_mulk_i32 s11, 0x90
	s_sub_i32 s10, s10, s11
	s_bfe_u32 s11, s10, 0x3001c
	s_add_i32 s11, s10, s11
	s_sext_i32_i16 s13, s11
	s_and_b32 s11, s11, 0xfff8
	s_sub_i32 s10, s10, s11
	s_sext_i32_i16 s10, s10
	s_add_i32 s60, s12, s10
	s_ashr_i32 s62, s13, 3
	s_mul_i32 s10, s62, 5
	s_cmp_lt_u32 s62, 12
	s_cbranch_scc0 .Lpn_hi1
	s_mov_b32 s12, 0x1ee6b16a
	s_mov_b32 s13, 0x398a48c
	s_branch .Lpn_go1
.Lpn_hi1:
	s_sub_i32 s10, s10, 60
	s_mov_b32 s12, 0x12818820
	s_mov_b32 s13, 0
